# f25 plus removal of the one dead small load in each of the proj Q and K variants (b4v in Q, bias2 in K) that sat ahead of their main tile loads
# speedup vs baseline: 1.0081x; 1.0081x over previous
.LBB0_3:
	s_andn2_b64 vcc, exec, s[12:13]
	s_cbranch_vccnz .LBB0_15
	v_lshlrev_b32_e32 v56, 2, v0
	v_mov_b32_e32 v57, 0
	s_waitcnt lgkmcnt(0)
	v_lshl_add_u64 v[2:3], s[6:7], 0, v[56:57]
	v_lshl_add_u64 v[4:5], s[16:17], 0, v[56:57]
	v_cmp_gt_u32_e32 vcc, 64, v0
	s_load_dwordx4 s[12:15], s[0:1], 0x28
	s_load_dwordx2 s[22:23], s[0:1], 0x8
	v_cndmask_b32_e32 v2, v4, v2, vcc
	v_cndmask_b32_e32 v3, v5, v3, vcc
	global_load_dword v54, v[2:3], off
	v_lshrrev_b32_e32 v2, 2, v0
	v_and_b32_e32 v70, 15, v0
	v_and_b32_e32 v55, 48, v2
	v_or_b32_e32 v66, v55, v70
	v_bfe_u32 v1, v0, 4, 2
	v_lshlrev_b32_e32 v2, 8, v66
	v_mov_b32_e32 v3, v57
	v_lshl_add_u64 v[2:3], s[8:9], 0, v[2:3]
	v_lshlrev_b32_e32 v4, 5, v1
	v_mov_b32_e32 v5, v57
	s_add_i32 s3, s3, -12
	s_lshl_b32 s18, s2, 1
	v_lshl_add_u64 v[2:3], v[2:3], 0, v[4:5]
	s_bfe_u32 s20, s2, 0x10002
	s_ashr_i32 s3, s3, 1
	s_and_b32 s18, s18, 6
	s_bfe_u32 s19, s2, 0x10003
	global_load_dwordx4 v[14:17], v[2:3], off
	v_lshl_add_u64 v[4:5], v[2:3], 0, 16
	s_mov_b64 s[8:9], 0x80
	s_or_b32 s19, s19, s18
	s_lshl_b32 s18, s3, 6
	s_mul_i32 s21, s20, 0x180
	global_load_dwordx4 v[18:21], v[4:5], off
	v_lshl_add_u64 v[4:5], v[2:3], 0, s[8:9]
	s_mov_b64 s[8:9], 0x90
	s_add_i32 s21, s18, s21
	s_lshl_b32 s20, s20, 3
	v_lshl_add_u64 v[2:3], v[2:3], 0, s[8:9]
	v_lshlrev_b32_e32 v22, 2, v55
	v_mov_b32_e32 v23, v57
	s_lshl_b32 s8, s19, 8
	global_load_dwordx4 v[6:9], v[4:5], off
	v_lshl_add_u64 v[24:25], s[10:11], 0, v[22:23]
	v_and_b32_e32 v72, 48, v0
	v_mov_b32_e32 v73, v57
	s_waitcnt lgkmcnt(0)
	s_add_u32 s8, s14, s8
	global_load_dwordx4 v[10:13], v[2:3], off
	v_lshl_add_u64 v[2:3], v[24:25], 0, v[72:73]
	s_addc_u32 s9, s15, 0
	global_load_dwordx4 v[2:5], v[2:3], off
	v_lshlrev_b32_e32 v26, 2, v70
	v_mov_b32_e32 v27, v57
	v_lshl_add_u64 v[22:23], s[8:9], 0, v[22:23]
	v_lshl_add_u64 v[24:25], v[24:25], 0, v[26:27]
	v_lshl_add_u64 v[22:23], v[22:23], 0, v[26:27]
	v_lshrrev_b32_e32 v71, 4, v0
	global_load_dword v67, v[22:23], off
	v_or_b32_e32 v22, s21, v71
	v_ashrrev_i32_e32 v23, 31, v22
	v_lshlrev_b64 v[22:23], 11, v[22:23]
	v_and_b32_e32 v73, 60, v56
	v_lshl_add_u64 v[22:23], s[22:23], 0, v[22:23]
	v_lshlrev_b32_e32 v56, 2, v73
	v_lshl_add_u64 v[62:63], v[22:23], 0, v[56:57]
	global_load_dwordx4 v[22:25], v[62:63], off
	s_mov_b32 s8, 0x10000
	v_add_co_u32_e32 v64, vcc, s8, v62
	v_lshlrev_b32_e32 v30, 9, v71
	s_nop 0
	v_addc_co_u32_e32 v65, vcc, 0, v63, vcc
	global_load_dwordx4 v[26:29], v[64:65], off
	v_lshl_or_b32 v30, s19, 15, v30
	v_mov_b32_e32 v31, v57
	v_lshl_add_u64 v[30:31], v[30:31], 2, s[12:13]
	v_lshl_add_u64 v[60:61], v[30:31], 0, v[56:57]
	global_load_dwordx4 v[30:33], v[60:61], off
	v_add_co_u32_e32 v58, vcc, s8, v60
	v_lshrrev_b32_e32 v56, 3, v0
	s_nop 0
	v_addc_co_u32_e32 v59, vcc, 0, v61, vcc
	global_load_dwordx4 v[34:37], v[58:59], off
	global_load_dwordx4 v[38:41], v[62:63], off offset:256
	global_load_dwordx4 v[42:45], v[64:65], off offset:256
	global_load_dwordx4 v[46:49], v[60:61], off offset:256
	global_load_dwordx4 v[50:53], v[58:59], off offset:256
	v_and_b32_e32 v69, 32, v56
	v_or_b32_e32 v56, v69, v70
	v_mul_u32_u24_e32 v70, 0xa0, v71
	v_lshl_add_u32 v71, v73, 1, v70
	s_movk_i32 s8, 0xa0
	s_or_b32 s12, s19, s20
	s_lshl_b32 s13, s12, 4
	v_cmp_lt_u32_e32 vcc, 63, v0
	s_waitcnt vmcnt(7)
	v_cvt_f16_f32_e32 v22, v22
	v_cvt_f16_f32_e32 v25, v25
	v_cvt_pk_f16_f32 v23, v23, v24
	v_pack_b32_f16 v74, v22, v23
	v_alignbit_b32 v75, v25, v23, 16
	global_load_dwordx4 v[22:25], v[62:63], off offset:512
	s_waitcnt vmcnt(7)
	v_cvt_f16_f32_e32 v26, v26
	v_cvt_f16_f32_e32 v73, v29
	v_cvt_pk_f16_f32 v70, v27, v28
	v_pack_b32_f16 v76, v26, v70
	global_load_dwordx4 v[26:29], v[64:65], off offset:512
	s_waitcnt vmcnt(7)
	v_cvt_f16_f32_e32 v30, v30
	v_alignbit_b32 v77, v73, v70, 16
	v_cvt_f16_f32_e32 v73, v33
	s_waitcnt vmcnt(6)
	v_cvt_f16_f32_e32 v34, v34
	v_cvt_f16_f32_e32 v37, v37
	v_cvt_pk_f16_f32 v70, v31, v32
	ds_write2st64_b64 v71, v[74:75], v[76:77] offset1:10
	v_pack_b32_f16 v74, v30, v70
	global_load_dwordx4 v[30:33], v[60:61], off offset:512
	v_cvt_pk_f16_f32 v35, v35, v36
	v_alignbit_b32 v75, v73, v70, 16
	v_pack_b32_f16 v34, v34, v35
	v_alignbit_b32 v35, v37, v35, 16
	ds_write2st64_b64 v71, v[74:75], v[34:35] offset0:60 offset1:70
	global_load_dwordx4 v[34:37], v[58:59], off offset:512
	v_mad_u32_u24 v70, v56, s8, v72
	s_waitcnt lgkmcnt(0)
	s_barrier
	ds_read_b128 v[74:77], v70
	s_waitcnt vmcnt(7)
	v_cvt_f16_f32_e32 v38, v38
	v_cvt_f16_f32_e32 v41, v41
	v_cvt_pk_f16_f32 v39, v39, v40
	v_mad_u32_u24 v72, v66, s8, v72
	v_pack_b32_f16 v38, v38, v39
	v_alignbit_b32 v39, v41, v39, 16
	s_waitcnt vmcnt(6)
	v_cvt_f16_f32_e32 v40, v42
	v_cvt_f16_f32_e32 v41, v45
	ds_read_b128 v[78:81], v72 offset:30720
	ds_read_b128 v[82:85], v70 offset:64
	ds_read_b128 v[86:89], v72 offset:30784
	v_cvt_pk_f16_f32 v42, v43, v44
	s_waitcnt lgkmcnt(2)
	v_mfma_f32_16x16x32_f16 v[74:77], v[74:77], v[78:81], 0
	ds_read_b128 v[90:93], v70 offset:2560
	ds_read_b128 v[94:97], v70 offset:2624
	v_pack_b32_f16 v40, v40, v42
	v_alignbit_b32 v41, v41, v42, 16
	global_load_dwordx4 v[42:45], v[62:63], off offset:768
	s_waitcnt lgkmcnt(2)
	v_mfma_f32_16x16x32_f16 v[74:77], v[82:85], v[86:89], v[74:77]
	s_waitcnt vmcnt(6)
	v_cvt_f16_f32_e32 v46, v46
	v_cvt_pk_f16_f32 v47, v47, v48
	v_cvt_f16_f32_e32 v48, v49
	s_waitcnt vmcnt(5)
	v_cvt_f16_f32_e32 v73, v50
	v_cvt_f16_f32_e32 v84, v53
	v_cvt_pk_f16_f32 v85, v51, v52
	global_load_dwordx4 v[50:53], v[64:65], off offset:768
	v_pack_b32_f16 v82, v46, v47
	v_alignbit_b32 v83, v48, v47, 16
	global_load_dwordx4 v[46:49], v[60:61], off offset:768
	ds_write2st64_b64 v71, v[38:39], v[40:41] offset0:20 offset1:30
	v_pack_b32_f16 v38, v73, v85
	v_alignbit_b32 v39, v84, v85, 16
	ds_write2st64_b64 v71, v[82:83], v[38:39] offset0:80 offset1:90
	global_load_dwordx4 v[38:41], v[58:59], off offset:768
	s_waitcnt lgkmcnt(0)
	s_barrier
	ds_read_b128 v[82:85], v70 offset:10240
	v_mfma_f32_16x16x32_f16 v[78:81], v[90:93], v[78:81], 0
	s_waitcnt vmcnt(7)
	v_cvt_f16_f32_e32 v22, v22
	v_mfma_f32_16x16x32_f16 v[78:81], v[94:97], v[86:89], v[78:81]
	ds_read_b128 v[86:89], v72 offset:40960
	ds_read_b128 v[90:93], v70 offset:10304
	ds_read_b128 v[94:97], v72 offset:41024
	v_cvt_f16_f32_e32 v25, v25
	v_cvt_pk_f16_f32 v23, v23, v24
	s_waitcnt lgkmcnt(2)
	v_mfma_f32_16x16x32_f16 v[74:77], v[82:85], v[86:89], v[74:77]
	ds_read_b128 v[82:85], v70 offset:12800
	ds_read_b128 v[98:101], v70 offset:12864
	s_waitcnt vmcnt(6)
	v_cvt_f16_f32_e32 v24, v29
	s_waitcnt vmcnt(4)
	v_cvt_f16_f32_e32 v34, v34
	s_waitcnt lgkmcnt(1)
	v_mfma_f32_16x16x32_f16 v[78:81], v[82:85], v[86:89], v[78:81]
	v_pack_b32_f16 v82, v22, v23
	v_cvt_f16_f32_e32 v22, v26
	v_alignbit_b32 v83, v25, v23, 16
	v_cvt_pk_f16_f32 v23, v27, v28
	v_alignbit_b32 v85, v24, v23, 16
	v_pack_b32_f16 v84, v22, v23
	v_cvt_f16_f32_e32 v26, v30
	v_cvt_f16_f32_e32 v27, v33
	global_load_dwordx4 v[22:25], v[62:63], off offset:1024
	v_cvt_pk_f16_f32 v28, v31, v32
	v_cvt_pk_f16_f32 v35, v35, v36
	v_cvt_f16_f32_e32 v36, v37
	v_pack_b32_f16 v86, v26, v28
	v_alignbit_b32 v87, v27, v28, 16
	global_load_dwordx4 v[26:29], v[64:65], off offset:1024
	v_pack_b32_f16 v34, v34, v35
	v_alignbit_b32 v35, v36, v35, 16
	global_load_dwordx4 v[30:33], v[60:61], off offset:1024
	ds_write2st64_b64 v71, v[86:87], v[34:35] offset0:60 offset1:70
	global_load_dwordx4 v[34:37], v[58:59], off offset:1024
	ds_write2st64_b64 v71, v[82:83], v[84:85] offset1:10
	s_waitcnt lgkmcnt(0)
	s_barrier
	ds_read_b128 v[82:85], v70
	v_mfma_f32_16x16x32_f16 v[74:77], v[90:93], v[94:97], v[74:77]
	s_waitcnt vmcnt(7)
	v_cvt_f16_f32_e32 v42, v42
	v_cvt_pk_f16_f32 v43, v43, v44
	v_cvt_f16_f32_e32 v45, v45
	v_mfma_f32_16x16x32_f16 v[78:81], v[98:101], v[94:97], v[78:81]
	ds_read_b128 v[86:89], v72 offset:30720
	ds_read_b128 v[90:93], v70 offset:64
	ds_read_b128 v[94:97], v72 offset:30784
	s_waitcnt vmcnt(6)
	v_cvt_pk_f16_f32 v44, v51, v52
	s_waitcnt vmcnt(5)
	v_cvt_pk_f16_f32 v47, v47, v48
	s_waitcnt lgkmcnt(2)
	v_mfma_f32_16x16x32_f16 v[74:77], v[82:85], v[86:89], v[74:77]
	ds_read_b128 v[82:85], v70 offset:2560
	ds_read_b128 v[98:101], v70 offset:2624
	s_waitcnt vmcnt(4)
	v_cvt_pk_f16_f32 v48, v39, v40
	s_waitcnt vmcnt(3)
	v_cvt_f16_f32_e32 v22, v22
	s_waitcnt lgkmcnt(1)
	v_mfma_f32_16x16x32_f16 v[78:81], v[82:85], v[86:89], v[78:81]
	v_pack_b32_f16 v82, v42, v43
	v_cvt_f16_f32_e32 v42, v50
	v_alignbit_b32 v83, v45, v43, 16
	v_cvt_f16_f32_e32 v43, v53
	v_mfma_f32_16x16x32_f16 v[74:77], v[90:93], v[94:97], v[74:77]
	v_pack_b32_f16 v50, v42, v44
	v_cvt_f16_f32_e32 v42, v46
	v_alignbit_b32 v51, v43, v44, 16
	v_cvt_f16_f32_e32 v46, v49
	ds_write2st64_b64 v71, v[82:83], v[50:51] offset0:20 offset1:30
	v_pack_b32_f16 v52, v42, v47
	global_load_dwordx4 v[42:45], v[62:63], off offset:1280
	v_alignbit_b32 v53, v46, v47, 16
	v_cvt_f16_f32_e32 v46, v38
	v_cvt_f16_f32_e32 v47, v41
	global_load_dwordx4 v[38:41], v[64:65], off offset:1280
	s_waitcnt lgkmcnt(1)
	v_mfma_f32_16x16x32_f16 v[78:81], v[98:101], v[94:97], v[78:81]
	v_pack_b32_f16 v84, v46, v48
	v_alignbit_b32 v85, v47, v48, 16
	global_load_dwordx4 v[46:49], v[60:61], off offset:1280
	ds_write2st64_b64 v71, v[52:53], v[84:85] offset0:80 offset1:90
	global_load_dwordx4 v[50:53], v[58:59], off offset:1280
	s_waitcnt lgkmcnt(0)
	s_barrier
	ds_read_b128 v[82:85], v70 offset:10240
	ds_read_b128 v[86:89], v72 offset:40960
	ds_read_b128 v[90:93], v70 offset:10304
	ds_read_b128 v[94:97], v72 offset:41024
	s_waitcnt lgkmcnt(2)
	v_mfma_f32_16x16x32_f16 v[74:77], v[82:85], v[86:89], v[74:77]
	ds_read_b128 v[82:85], v70 offset:12800
	ds_read_b128 v[98:101], v70 offset:12864
	v_cvt_pk_f16_f32 v73, v23, v24
	s_waitcnt vmcnt(6)
	v_cvt_f16_f32_e32 v26, v26
	s_waitcnt lgkmcnt(1)
	v_mfma_f32_16x16x32_f16 v[78:81], v[82:85], v[86:89], v[78:81]
	v_cvt_f16_f32_e32 v83, v25
	v_pack_b32_f16 v82, v22, v73
	global_load_dwordx4 v[22:25], v[62:63], off offset:1536
	v_cvt_f16_f32_e32 v85, v29
	v_alignbit_b32 v83, v83, v73, 16
	v_cvt_pk_f16_f32 v73, v27, v28
	v_pack_b32_f16 v84, v26, v73
	global_load_dwordx4 v[26:29], v[64:65], off offset:1536
	v_alignbit_b32 v85, v85, v73, 16
	s_waitcnt vmcnt(7)
	v_cvt_f16_f32_e32 v73, v30
	v_cvt_f16_f32_e32 v87, v33
	s_waitcnt vmcnt(6)
	v_cvt_f16_f32_e32 v34, v34
	v_cvt_pk_f16_f32 v88, v31, v32
	v_cvt_pk_f16_f32 v89, v35, v36
	global_load_dwordx4 v[30:33], v[60:61], off offset:1536
	v_pack_b32_f16 v86, v73, v88
	v_alignbit_b32 v87, v87, v88, 16
	v_cvt_f16_f32_e32 v73, v37
	v_pack_b32_f16 v88, v34, v89
	global_load_dwordx4 v[34:37], v[58:59], off offset:1536
	ds_write2st64_b64 v71, v[82:83], v[84:85] offset1:10
	v_alignbit_b32 v89, v73, v89, 16
	ds_write2st64_b64 v71, v[86:87], v[88:89] offset0:60 offset1:70
	s_waitcnt lgkmcnt(0)
	s_barrier
	global_load_dwordx4 v[82:85], v[62:63], off offset:1792
	ds_read_b128 v[86:89], v70
	global_load_dwordx4 v[62:65], v[64:65], off offset:1792
	v_mfma_f32_16x16x32_f16 v[74:77], v[90:93], v[94:97], v[74:77]
	s_waitcnt vmcnt(9)
	v_cvt_pk_f16_f32 v73, v43, v44
	v_mfma_f32_16x16x32_f16 v[78:81], v[98:101], v[94:97], v[78:81]
	ds_read_b128 v[90:93], v72 offset:30720
	ds_read_b128 v[94:97], v70 offset:64
	ds_read_b128 v[98:101], v72 offset:30784
	s_waitcnt vmcnt(8)
	v_cvt_f16_f32_e32 v41, v41
	s_waitcnt lgkmcnt(2)
	v_mfma_f32_16x16x32_f16 v[74:77], v[86:89], v[90:93], v[74:77]
	ds_read_b128 v[86:89], v70 offset:2560
	ds_read_b128 v[102:105], v70 offset:2624
	s_waitcnt vmcnt(7)
	v_cvt_f16_f32_e32 v46, v46
	s_waitcnt lgkmcnt(1)
	v_mfma_f32_16x16x32_f16 v[78:81], v[86:89], v[90:93], v[78:81]
	global_load_dwordx4 v[86:89], v[60:61], off offset:1792
	v_cvt_f16_f32_e32 v60, v42
	v_cvt_f16_f32_e32 v61, v45
	global_load_dwordx4 v[42:45], v[58:59], off offset:1792
	v_cvt_f16_f32_e32 v49, v49
	v_cvt_pk_f16_f32 v47, v47, v48
	v_cvt_f16_f32_e32 v90, v38
	v_pack_b32_f16 v46, v46, v47
	s_waitcnt vmcnt(8)
	v_cvt_f16_f32_e32 v48, v50
	v_alignbit_b32 v47, v49, v47, 16
	v_cvt_f16_f32_e32 v49, v53
	v_pack_b32_f16 v38, v60, v73
	v_cvt_pk_f16_f32 v91, v39, v40
	v_cvt_pk_f16_f32 v50, v51, v52
	v_alignbit_b32 v39, v61, v73, 16
	v_pack_b32_f16 v40, v90, v91
	v_alignbit_b32 v41, v41, v91, 16
	v_pack_b32_f16 v48, v48, v50
	v_alignbit_b32 v49, v49, v50, 16
	ds_write2st64_b64 v71, v[38:39], v[40:41] offset0:20 offset1:30
	s_waitcnt vmcnt(7)
	v_cvt_f16_f32_e32 v22, v22
	v_cvt_f16_f32_e32 v25, v25
	v_cvt_pk_f16_f32 v23, v23, v24
	ds_write2st64_b64 v71, v[46:47], v[48:49] offset0:80 offset1:90
	v_pack_b32_f16 v58, v22, v23
	s_waitcnt vmcnt(6)
	v_cvt_f16_f32_e32 v22, v26
	v_alignbit_b32 v59, v25, v23, 16
	v_cvt_pk_f16_f32 v23, v27, v28
	v_cvt_f16_f32_e32 v24, v29
	v_pack_b32_f16 v60, v22, v23
	s_waitcnt lgkmcnt(0)
	s_barrier
	s_waitcnt vmcnt(5)
	v_cvt_f16_f32_e32 v22, v30
	v_cvt_f16_f32_e32 v25, v33
	v_alignbit_b32 v61, v24, v23, 16
	v_cvt_pk_f16_f32 v23, v31, v32
	v_pack_b32_f16 v90, v22, v23
	s_waitcnt vmcnt(4)
	v_cvt_f16_f32_e32 v26, v34
	v_cvt_f16_f32_e32 v27, v37
	v_cvt_pk_f16_f32 v28, v35, v36
	v_alignbit_b32 v91, v25, v23, 16
	v_mfma_f32_16x16x32_f16 v[22:25], v[102:105], v[98:101], v[78:81]
	s_waitcnt vmcnt(3)
	v_cvt_f16_f32_e32 v30, v82
	s_nop 0
	v_pack_b32_f16 v78, v26, v28
	v_alignbit_b32 v79, v27, v28, 16
	ds_read_b128 v[26:29], v70 offset:10240
	v_cvt_f16_f32_e32 v31, v85
	s_waitcnt vmcnt(2)
	v_cvt_f16_f32_e32 v50, v62
	v_cvt_pk_f16_f32 v32, v83, v84
	v_cvt_pk_f16_f32 v63, v63, v64
	v_mfma_f32_16x16x32_f16 v[74:77], v[94:97], v[98:101], v[74:77]
	v_pack_b32_f16 v80, v30, v32
	v_alignbit_b32 v81, v31, v32, 16
	ds_read_b128 v[30:33], v72 offset:40960
	ds_read_b128 v[34:37], v70 offset:12800
	ds_read_b128 v[38:41], v70 offset:10304
	ds_read_b128 v[46:49], v72 offset:41024
	v_pack_b32_f16 v62, v50, v63
	ds_read_b128 v[50:53], v70 offset:12864
	s_waitcnt lgkmcnt(4)
	v_mfma_f32_16x16x32_f16 v[26:29], v[26:29], v[30:33], v[74:77]
	ds_write2st64_b64 v71, v[58:59], v[60:61] offset1:10
	ds_write2st64_b64 v71, v[90:91], v[78:79] offset0:60 offset1:70
	s_waitcnt lgkmcnt(0)
	s_barrier
	v_mfma_f32_16x16x32_f16 v[22:25], v[34:37], v[30:33], v[22:25]
	ds_read_b128 v[30:33], v70
	v_cvt_f16_f32_e32 v64, v65
	v_mfma_f32_16x16x32_f16 v[26:29], v[38:41], v[46:49], v[26:29]
	ds_read_b128 v[34:37], v70 offset:2560
	ds_read_b128 v[38:41], v72 offset:30720
	v_alignbit_b32 v63, v64, v63, 16
	v_mfma_f32_16x16x32_f16 v[22:25], v[50:53], v[46:49], v[22:25]
	ds_read_b128 v[46:49], v70 offset:64
	ds_read_b128 v[50:53], v72 offset:30784
	s_waitcnt vmcnt(1)
	v_cvt_f16_f32_e32 v58, v86
	v_cvt_f16_f32_e32 v60, v89
	s_waitcnt lgkmcnt(2)
	v_mfma_f32_16x16x32_f16 v[22:25], v[34:37], v[38:41], v[22:25]
	s_waitcnt vmcnt(0)
	v_cvt_f16_f32_e32 v36, v42
	v_cvt_f16_f32_e32 v37, v45
	v_cvt_pk_f16_f32 v59, v87, v88
	v_mfma_f32_16x16x32_f16 v[26:29], v[30:33], v[38:41], v[26:29]
	ds_read_b128 v[30:33], v70 offset:2624
	v_cvt_pk_f16_f32 v38, v43, v44
	v_pack_b32_f16 v34, v58, v59
	v_alignbit_b32 v35, v60, v59, 16
	v_pack_b32_f16 v36, v36, v38
	v_alignbit_b32 v37, v37, v38, 16
	ds_write2st64_b64 v71, v[80:81], v[62:63] offset0:20 offset1:30
	ds_write2st64_b64 v71, v[34:35], v[36:37] offset0:80 offset1:90
	s_waitcnt lgkmcnt(0)
	s_barrier
	ds_read_b128 v[34:37], v70 offset:10240
	v_mfma_f32_16x16x32_f16 v[26:29], v[46:49], v[50:53], v[26:29]
	v_mfma_f32_16x16x32_f16 v[22:25], v[30:33], v[50:53], v[22:25]
	ds_read_b128 v[30:33], v72 offset:40960
	ds_read_b128 v[38:41], v70 offset:10304
	ds_read_b128 v[42:45], v72 offset:41024
	s_waitcnt lgkmcnt(2)
	v_mfma_f32_16x16x32_f16 v[26:29], v[34:37], v[30:33], v[26:29]
	ds_read_b128 v[34:37], v70 offset:12800
	ds_read_b128 v[46:49], v70 offset:12864
	s_waitcnt vmcnt(0)
	s_waitcnt lgkmcnt(0)
	v_mfma_f32_16x16x32_f16 v[22:25], v[34:37], v[30:33], v[22:25]
	v_lshl_or_b32 v30, v1, 2, v69
	v_mul_u32_u24_e32 v30, 0xa0, v30
	v_lshl_add_u32 v30, v66, 1, v30
	v_mfma_f32_16x16x32_f16 v[26:29], v[38:41], v[42:45], v[26:29]
	v_cvt_pk_f16_f32 v21, v20, v21
	v_cvt_pk_f16_f32 v20, v18, v19
	v_cvt_pk_f16_f32 v19, v16, v17
	v_mfma_f32_16x16x32_f16 v[22:25], v[46:49], v[42:45], v[22:25]
	v_cvt_pk_f16_f32 v18, v14, v15
	s_nop 2
	v_add_f32_e32 v26, v26, v67
	v_cvt_f16_f32_e32 v26, v26
	v_add_f32_e32 v27, v27, v67
	v_cvt_f16_f32_e32 v27, v27
	v_add_f32_e32 v22, v22, v67
	v_cvt_f16_f32_e32 v22, v22
	v_add_f32_e32 v23, v23, v67
	v_add_f32_e32 v28, v28, v67
	v_cvt_f16_f32_e32 v23, v23
	v_add_f32_e32 v24, v24, v67
	v_cvt_f16_f32_e32 v28, v28
	v_add_f32_e32 v29, v29, v67
	v_cvt_f16_f32_e32 v24, v24
	v_add_f32_e32 v25, v25, v67
	v_cvt_f16_f32_e32 v29, v29
	v_cvt_f16_f32_e32 v25, v25
	s_barrier
	ds_write_b16 v30, v26
	ds_write_b16 v30, v27 offset:160
	ds_write_b16 v30, v28 offset:320
	ds_write_b16 v30, v29 offset:480
	ds_write_b16 v30, v22 offset:2560
	ds_write_b16 v30, v23 offset:2720
	ds_write_b16 v30, v24 offset:2880
	ds_write_b16 v30, v25 offset:3040
	s_waitcnt lgkmcnt(0)
	s_barrier
	ds_read_b128 v[14:17], v70
	ds_read_b128 v[22:25], v70 offset:64
	v_cvt_pk_f16_f32 v13, v12, v13
	v_cvt_pk_f16_f32 v12, v10, v11
	v_cvt_pk_f16_f32 v11, v8, v9
	v_cvt_pk_f16_f32 v10, v6, v7
	s_waitcnt lgkmcnt(1)
	v_mfma_f32_16x16x32_f16 v[14:17], v[18:21], v[14:17], 0
	ds_read_b128 v[26:29], v70 offset:2560
	ds_read_b128 v[30:33], v70 offset:2624
	s_load_dwordx2 s[10:11], s[0:1], 0x70
	s_load_dwordx2 s[8:9], s[0:1], 0x98
	s_waitcnt lgkmcnt(0)
	v_mfma_f32_16x16x32_f16 v[6:9], v[10:13], v[22:25], v[14:17]
	v_or_b32_e32 v22, s18, v56
	v_ashrrev_i32_e32 v23, 31, v22
	s_nop 0
	v_lshrrev_b32_e32 v14, 2, v55
	v_or3_b32 v1, s13, v14, v1
	v_mfma_f32_16x16x32_f16 v[18:21], v[18:21], v[26:29], 0
	v_mul_u32_u24_e32 v56, 0x180, v1
	s_nop 0
	v_add_f32_e32 v1, v2, v6
	s_mov_b32 s13, 0xc2200000
	v_mov_b32_e32 v28, 0x42200000
	v_med3_f32 v1, v1, s13, v28
	v_mul_f32_e32 v1, 0x4038aa3b, v1
	v_exp_f32_e32 v6, v1
	v_add_f32_e32 v1, v3, v7
	v_med3_f32 v1, v1, s13, v28
	v_mul_f32_e32 v1, 0x4038aa3b, v1
	v_exp_f32_e32 v7, v1
	v_add_f32_e32 v1, v4, v8
	v_med3_f32 v1, v1, s13, v28
	v_mul_f32_e32 v1, 0x4038aa3b, v1
	v_exp_f32_e32 v8, v1
	v_add_f32_e32 v1, v5, v9
	v_med3_f32 v1, v1, s13, v28
	v_mul_f32_e32 v1, 0x4038aa3b, v1
	v_exp_f32_e32 v9, v1
	v_cvt_f16_f32_e32 v1, v6
	v_lshl_add_u64 v[24:25], v[56:57], 0, v[22:23]
	v_lshl_add_u64 v[14:15], v[24:25], 4, s[10:11]
	global_store_dwordx4 v[14:15], v[6:9], off sc0 sc1
	v_pack_b32_f16 v14, 1.0, v1
	v_cvt_f16_f32_e32 v1, v9
	v_mfma_f32_16x16x32_f16 v[10:13], v[10:13], v[30:33], v[18:21]
	v_mul_f32_e32 v16, v6, v7
	v_mov_b32_e32 v17, v8
	v_pk_mul_f32 v[26:27], v[6:7], v[8:9] op_sel_hi:[1,0]
	v_mov_b32_e32 v20, v9
	v_pk_mul_f32 v[18:19], v[6:7], v[20:21] op_sel_hi:[1,0]
	v_mul_f32_e32 v23, v8, v16
	v_cvt_pk_f16_f32 v15, v7, v16
	v_cvt_pk_f16_f32 v19, v18, v19
	v_pk_mul_f32 v[16:17], v[20:21], v[16:17] op_sel_hi:[0,1]
	v_pk_mul_f32 v[20:21], v[20:21], v[26:27] op_sel_hi:[0,1]
	v_pack_b32_f16 v18, v1, v19
	v_cvt_pk_f16_f32 v1, v16, v17
	v_cvt_pk_f16_f32 v21, v20, v21
	v_alignbit_b32 v19, v1, v19, 16
	v_alignbit_b32 v20, v21, v1, 16
	v_add_f32_e32 v1, v2, v10
	v_med3_f32 v1, v1, s13, v28
	v_mul_f32_e32 v1, 0x4038aa3b, v1
	v_exp_f32_e32 v2, v1
	v_add_f32_e32 v1, v3, v11
	v_med3_f32 v1, v1, s13, v28
	v_mul_f32_e32 v1, 0x4038aa3b, v1
	v_exp_f32_e32 v3, v1
	v_add_f32_e32 v1, v4, v12
	v_med3_f32 v1, v1, s13, v28
	v_mul_f32_e32 v1, 0x4038aa3b, v1
	v_exp_f32_e32 v4, v1
	v_add_f32_e32 v1, v5, v13
	v_lshlrev_b64 v[24:25], 5, v[24:25]
	v_med3_f32 v1, v1, s13, v28
	v_cvt_pk_f16_f32 v16, v8, v26
	v_cvt_pk_f16_f32 v17, v27, v23
	v_lshrrev_b32_e32 v21, 16, v21
	v_lshl_add_u64 v[24:25], s[8:9], 0, v[24:25]
	v_mul_f32_e32 v1, 0x4038aa3b, v1
	v_fma_mixhi_f16 v21, v9, v23, 0
	global_store_dwordx4 v[24:25], v[14:17], off
	global_store_dwordx4 v[24:25], v[18:21], off offset:16
	v_exp_f32_e32 v5, v1
	v_or_b32_e32 v14, 16, v22
	v_cvt_f16_f32_e32 v1, v2
	v_ashrrev_i32_e32 v15, 31, v14
	v_lshl_add_u64 v[18:19], v[56:57], 0, v[14:15]
	v_lshl_add_u64 v[10:11], v[18:19], 4, s[10:11]
	global_store_dwordx4 v[10:11], v[2:5], off sc0 sc1
	v_pack_b32_f16 v10, 1.0, v1
	v_cvt_f16_f32_e32 v1, v5
	v_mov_b32_e32 v16, v5
	v_mul_f32_e32 v12, v2, v3
	v_pk_mul_f32 v[14:15], v[2:3], v[16:17] op_sel_hi:[1,0]
	v_mov_b32_e32 v13, v4
	v_pk_mul_f32 v[20:21], v[2:3], v[4:5] op_sel_hi:[1,0]
	v_mul_f32_e32 v22, v4, v12
	v_cvt_pk_f16_f32 v11, v3, v12
	v_cvt_pk_f16_f32 v15, v14, v15
	v_pk_mul_f32 v[12:13], v[16:17], v[12:13] op_sel_hi:[0,1]
	v_pk_mul_f32 v[16:17], v[16:17], v[20:21] op_sel_hi:[0,1]
	v_pack_b32_f16 v14, v1, v15
	v_cvt_pk_f16_f32 v1, v12, v13
	v_cvt_pk_f16_f32 v17, v16, v17
	v_lshlrev_b64 v[18:19], 5, v[18:19]
	v_alignbit_b32 v15, v1, v15, 16
	v_cvt_pk_f16_f32 v12, v4, v20
	v_cvt_pk_f16_f32 v13, v21, v22
	v_alignbit_b32 v16, v17, v1, 16
	v_lshrrev_b32_e32 v17, 16, v17
	v_lshl_add_u64 v[18:19], s[8:9], 0, v[18:19]
	v_fma_mixhi_f16 v17, v5, v22, 0
	global_store_dwordx4 v[18:19], v[10:13], off
	global_store_dwordx4 v[18:19], v[14:17], off offset:16
	s_and_saveexec_b64 s[8:9], vcc
	s_xor_b64 s[8:9], exec, s[8:9]
	s_cbranch_execz .LBB0_6
	v_mbcnt_lo_u32_b32 v1, -1, 0
	v_mbcnt_hi_u32_b32 v1, -1, v1
	v_and_b32_e32 v10, 64, v1
	v_add_u32_e32 v14, 64, v10
	v_xor_b32_e32 v15, 32, v1
	v_xor_b32_e32 v16, 16, v1
	v_xor_b32_e32 v18, 8, v1
	v_xor_b32_e32 v19, 4, v1
	v_xor_b32_e32 v20, 2, v1
	v_xor_b32_e32 v21, 1, v1

.LBB0_16:
	s_andn2_b64 vcc, exec, s[8:9]
	s_cbranch_vccnz .LBB0_27
	v_lshlrev_b32_e32 v24, 2, v0
	v_mov_b32_e32 v25, 0
	v_lshrrev_b32_e32 v1, 2, v0
	s_load_dwordx4 s[12:15], s[0:1], 0x48
	s_load_dwordx4 s[8:11], s[0:1], 0x18
	s_load_dwordx2 s[18:19], s[0:1], 0x0
	v_and_b32_e32 v26, 15, v0
	s_waitcnt lgkmcnt(0)
	v_lshl_add_u64 v[2:3], s[6:7], 0, v[24:25]
	v_lshl_add_u64 v[4:5], s[16:17], 0, v[24:25]
	v_cmp_gt_u32_e32 vcc, 64, v0
	v_and_b32_e32 v18, 48, v1
	v_or_b32_e32 v1, v18, v26
	v_cndmask_b32_e32 v3, v5, v3, vcc
	v_cndmask_b32_e32 v2, v4, v2, vcc
	v_bfe_u32 v23, v0, 4, 2
	global_load_dword v22, v[2:3], off
	v_lshlrev_b32_e32 v2, 8, v1
	v_mov_b32_e32 v3, v25
	v_lshl_add_u64 v[2:3], s[12:13], 0, v[2:3]
	v_lshlrev_b32_e32 v4, 5, v23
	v_mov_b32_e32 v5, v25
	s_lshl_b32 s3, s2, 1
	v_lshl_add_u64 v[10:11], v[2:3], 0, v[4:5]
	s_bfe_u32 s21, s2, 0x10002
	s_lshr_b32 s20, s2, 4
	s_and_b32 s3, s3, 6
	s_bfe_u32 s2, s2, 0x10003
	global_load_dwordx4 v[6:9], v[10:11], off
	v_lshl_add_u64 v[2:3], v[10:11], 0, 16
	s_mov_b64 s[6:7], 0x80
	s_or_b32 s3, s2, s3
	s_lshl_b32 s2, s20, 6
	s_mul_i32 s22, s21, 0x180
	global_load_dwordx4 v[14:17], v[2:3], off
	v_lshl_add_u64 v[2:3], v[10:11], 0, s[6:7]
	s_mov_b64 s[6:7], 0x90
	s_add_i32 s22, s22, s2
	s_lshl_b32 s21, s21, 3
	v_lshl_add_u64 v[10:11], v[10:11], 0, s[6:7]
	v_lshlrev_b32_e32 v28, 2, v18
	v_mov_b32_e32 v29, v25
	s_lshl_b32 s6, s3, 8
	global_load_dwordx4 v[2:5], v[2:3], off
	v_lshl_add_u64 v[30:31], s[14:15], 0, v[28:29]
	v_and_b32_e32 v64, 48, v0
	v_mov_b32_e32 v65, v25
	s_add_u32 s6, s10, s6
	global_load_dwordx4 v[10:13], v[10:11], off
	v_lshl_add_u64 v[18:19], v[30:31], 0, v[64:65]
	s_addc_u32 s7, s11, 0
	v_lshlrev_b32_e32 v32, 2, v26
	v_mov_b32_e32 v33, v25
	v_lshl_add_u64 v[28:29], s[6:7], 0, v[28:29]
	v_lshrrev_b32_e32 v60, 4, v0
	v_lshl_add_u64 v[30:31], v[30:31], 0, v[32:33]
	global_load_dword v96, v[30:31], off
	v_lshl_add_u64 v[28:29], v[28:29], 0, v[32:33]
	v_or_b32_e32 v27, s22, v60
	global_load_dword v97, v[28:29], off
	v_lshlrev_b32_e32 v28, 11, v27
	v_mov_b32_e32 v29, v25
	v_and_b32_e32 v61, 60, v24
	v_lshl_add_u64 v[28:29], s[18:19], 0, v[28:29]
	v_lshlrev_b32_e32 v24, 2, v61
	v_lshl_add_u64 v[88:89], v[28:29], 0, v[24:25]
	global_load_dwordx4 v[28:31], v[88:89], off
	s_mov_b32 s6, 0x10000
	v_add_co_u32_e32 v90, vcc, s6, v88
	v_lshlrev_b32_e32 v27, 9, v60
	s_nop 0
	v_addc_co_u32_e32 v91, vcc, 0, v89, vcc
	global_load_dwordx4 v[32:35], v[90:91], off
	v_lshl_or_b32 v36, s3, 15, v27
	v_mov_b32_e32 v37, v25
	v_lshl_add_u64 v[36:37], v[36:37], 2, s[8:9]
	v_lshl_add_u64 v[92:93], v[36:37], 0, v[24:25]
	global_load_dwordx4 v[36:39], v[92:93], off
	v_add_co_u32_e32 v94, vcc, s6, v92
	v_lshrrev_b32_e32 v24, 3, v0
	s_nop 0
	v_addc_co_u32_e32 v95, vcc, 0, v93, vcc
	global_load_dwordx4 v[40:43], v[94:95], off
	global_load_dwordx4 v[44:47], v[88:89], off offset:256
	global_load_dwordx4 v[48:51], v[90:91], off offset:256
	global_load_dwordx4 v[52:55], v[92:93], off offset:256
	global_load_dwordx4 v[56:59], v[94:95], off offset:256
	v_and_b32_e32 v24, 32, v24
	v_or_b32_e32 v62, v24, v26
	s_movk_i32 s6, 0xa0
	v_mad_u32_u24 v99, v62, s6, v64
	v_mad_u32_u24 v100, v1, s6, v64
	v_lshlrev_b32_e32 v23, 2, v23
	s_load_dwordx2 s[0:1], s[0:1], 0x68
	s_or_b32 s6, s3, s21
	v_cmp_lt_u32_e32 vcc, 63, v0
	s_waitcnt vmcnt(7)
	v_cvt_f16_f32_e32 v27, v28
	v_cvt_f16_f32_e32 v28, v31
	v_cvt_pk_f16_f32 v29, v29, v30
	v_pack_b32_f16 v26, v27, v29
	v_alignbit_b32 v27, v28, v29, 16
	v_mul_u32_u24_e32 v28, 0xa0, v60
	s_waitcnt vmcnt(6)
	v_cvt_f16_f32_e32 v29, v32
	v_cvt_f16_f32_e32 v30, v35
	v_cvt_pk_f16_f32 v31, v33, v34
	v_lshl_add_u32 v98, v61, 1, v28
	v_pack_b32_f16 v28, v29, v31
	v_alignbit_b32 v29, v30, v31, 16
	s_waitcnt vmcnt(5)
	v_cvt_f16_f32_e32 v30, v36
	ds_write2st64_b64 v98, v[26:27], v[28:29] offset1:10
	v_cvt_pk_f16_f32 v27, v37, v38
	v_cvt_f16_f32_e32 v28, v39
	v_pack_b32_f16 v26, v30, v27
	s_waitcnt vmcnt(4)
	v_cvt_f16_f32_e32 v29, v40
	v_cvt_f16_f32_e32 v30, v43
	v_cvt_pk_f16_f32 v31, v41, v42
	v_alignbit_b32 v27, v28, v27, 16
	v_pack_b32_f16 v28, v29, v31
	v_alignbit_b32 v29, v30, v31, 16
	ds_write2st64_b64 v98, v[26:27], v[28:29] offset0:60 offset1:70
	global_load_dwordx4 v[26:29], v[88:89], off offset:512
	global_load_dwordx4 v[30:33], v[90:91], off offset:512
	global_load_dwordx4 v[34:37], v[92:93], off offset:512
	global_load_dwordx4 v[38:41], v[94:95], off offset:512
	s_waitcnt vmcnt(7)
	v_cvt_f16_f32_e32 v42, v44
	v_cvt_pk_f16_f32 v43, v45, v46
	v_cvt_f16_f32_e32 v44, v47
	s_waitcnt vmcnt(6)
	v_cvt_f16_f32_e32 v45, v48
	v_cvt_f16_f32_e32 v47, v51
	v_cvt_pk_f16_f32 v46, v49, v50
	s_waitcnt vmcnt(5)
	v_cvt_f16_f32_e32 v48, v52
	v_cvt_pk_f16_f32 v49, v53, v54
	v_cvt_f16_f32_e32 v50, v55
	s_waitcnt vmcnt(4)
	v_cvt_f16_f32_e32 v51, v56
	v_cvt_f16_f32_e32 v53, v59
	v_cvt_pk_f16_f32 v52, v57, v58
	v_pack_b32_f16 v42, v42, v43
	v_alignbit_b32 v43, v44, v43, 16
	v_pack_b32_f16 v44, v45, v46
	v_alignbit_b32 v45, v47, v46, 16
	s_waitcnt lgkmcnt(0)
	s_barrier
	ds_read_b128 v[60:63], v99
	ds_read_b128 v[64:67], v100 offset:30720
	ds_read_b128 v[68:71], v99 offset:64
	ds_read_b128 v[72:75], v100 offset:30784
	ds_read_b128 v[76:79], v99 offset:2560
	ds_read_b128 v[80:83], v99 offset:2624
	v_pack_b32_f16 v46, v48, v49
	v_alignbit_b32 v47, v50, v49, 16
	v_pack_b32_f16 v48, v51, v52
	v_alignbit_b32 v49, v53, v52, 16
	ds_write2st64_b64 v98, v[42:43], v[44:45] offset0:20 offset1:30
	ds_write2st64_b64 v98, v[46:47], v[48:49] offset0:80 offset1:90
	global_load_dwordx4 v[42:45], v[88:89], off offset:768
	global_load_dwordx4 v[46:49], v[90:91], off offset:768
	global_load_dwordx4 v[50:53], v[92:93], off offset:768
	global_load_dwordx4 v[54:57], v[94:95], off offset:768
	s_waitcnt lgkmcnt(6)
	v_mfma_f32_16x16x32_f16 v[60:63], v[60:63], v[64:67], 0
	s_waitcnt lgkmcnt(0)
	s_barrier
	v_mfma_f32_16x16x32_f16 v[60:63], v[68:71], v[72:75], v[60:63]
	ds_read_b128 v[68:71], v99 offset:10240
	s_waitcnt vmcnt(7)
	v_cvt_f16_f32_e32 v26, v26
	v_mfma_f32_16x16x32_f16 v[64:67], v[76:79], v[64:67], 0
	v_cvt_pk_f16_f32 v27, v27, v28
	v_cvt_f16_f32_e32 v28, v29
	s_waitcnt vmcnt(6)
	v_cvt_f16_f32_e32 v29, v30
	v_cvt_pk_f16_f32 v30, v31, v32
	v_cvt_f16_f32_e32 v31, v33
	s_waitcnt vmcnt(5)
	v_cvt_f16_f32_e32 v32, v34
	v_cvt_pk_f16_f32 v33, v35, v36
	v_cvt_f16_f32_e32 v34, v37
	s_waitcnt vmcnt(4)
	v_cvt_f16_f32_e32 v35, v38
	v_cvt_f16_f32_e32 v37, v41
	v_mfma_f32_16x16x32_f16 v[64:67], v[80:83], v[72:75], v[64:67]
	ds_read_b128 v[72:75], v100 offset:40960
	ds_read_b128 v[76:79], v99 offset:10304
	ds_read_b128 v[80:83], v100 offset:41024
	v_cvt_pk_f16_f32 v36, v39, v40
	v_pack_b32_f16 v26, v26, v27
	v_alignbit_b32 v27, v28, v27, 16
	v_pack_b32_f16 v28, v29, v30
	v_alignbit_b32 v29, v31, v30, 16
	s_waitcnt lgkmcnt(2)
	v_mfma_f32_16x16x32_f16 v[58:61], v[68:71], v[72:75], v[60:63]
	ds_read_b128 v[68:71], v99 offset:12800
	ds_read_b128 v[84:87], v99 offset:12864
	v_pack_b32_f16 v30, v32, v33
	v_alignbit_b32 v31, v34, v33, 16
	v_pack_b32_f16 v32, v35, v36
	v_alignbit_b32 v33, v37, v36, 16
	ds_write2st64_b64 v98, v[26:27], v[28:29] offset1:10
	ds_write2st64_b64 v98, v[30:31], v[32:33] offset0:60 offset1:70
	global_load_dwordx4 v[26:29], v[88:89], off offset:1024
	global_load_dwordx4 v[30:33], v[90:91], off offset:1024
	global_load_dwordx4 v[34:37], v[92:93], off offset:1024
	global_load_dwordx4 v[38:41], v[94:95], off offset:1024
	s_waitcnt lgkmcnt(3)
	v_mfma_f32_16x16x32_f16 v[62:65], v[68:71], v[72:75], v[64:67]
	s_waitcnt lgkmcnt(0)
	s_barrier
	s_nop 0
	ds_read_b128 v[66:69], v99
	s_waitcnt vmcnt(7)
	v_cvt_f16_f32_e32 v42, v42
	v_cvt_pk_f16_f32 v43, v43, v44
	v_cvt_f16_f32_e32 v44, v45
	s_waitcnt vmcnt(6)
	v_cvt_f16_f32_e32 v45, v46
	v_cvt_pk_f16_f32 v46, v47, v48
	v_cvt_f16_f32_e32 v47, v49
	v_mfma_f32_16x16x32_f16 v[58:61], v[76:79], v[80:83], v[58:61]
	s_waitcnt vmcnt(5)
	v_cvt_f16_f32_e32 v48, v50
	v_cvt_pk_f16_f32 v49, v51, v52
	v_cvt_f16_f32_e32 v50, v53
	s_waitcnt vmcnt(4)
	v_cvt_f16_f32_e32 v51, v54
	v_cvt_f16_f32_e32 v53, v57
	v_mfma_f32_16x16x32_f16 v[62:65], v[84:87], v[80:83], v[62:65]
	ds_read_b128 v[70:73], v100 offset:30720
	ds_read_b128 v[74:77], v99 offset:64
	ds_read_b128 v[78:81], v100 offset:30784
	v_cvt_pk_f16_f32 v52, v55, v56
	v_pack_b32_f16 v42, v42, v43
	v_alignbit_b32 v43, v44, v43, 16
	v_pack_b32_f16 v44, v45, v46
	v_alignbit_b32 v45, v47, v46, 16
	s_waitcnt lgkmcnt(2)
	v_mfma_f32_16x16x32_f16 v[58:61], v[66:69], v[70:73], v[58:61]
	ds_read_b128 v[66:69], v99 offset:2560
	ds_read_b128 v[82:85], v99 offset:2624
	v_pack_b32_f16 v46, v48, v49
	v_alignbit_b32 v47, v50, v49, 16
	v_pack_b32_f16 v48, v51, v52
	v_alignbit_b32 v49, v53, v52, 16
	ds_write2st64_b64 v98, v[42:43], v[44:45] offset0:20 offset1:30
	ds_write2st64_b64 v98, v[46:47], v[48:49] offset0:80 offset1:90
	global_load_dwordx4 v[42:45], v[88:89], off offset:1280
	global_load_dwordx4 v[46:49], v[90:91], off offset:1280
	global_load_dwordx4 v[50:53], v[92:93], off offset:1280
	global_load_dwordx4 v[54:57], v[94:95], off offset:1280
	s_waitcnt lgkmcnt(3)
	v_mfma_f32_16x16x32_f16 v[62:65], v[66:69], v[70:73], v[62:65]
	s_waitcnt lgkmcnt(0)
	s_barrier
	ds_read_b128 v[66:69], v99 offset:10240
	v_mfma_f32_16x16x32_f16 v[58:61], v[74:77], v[78:81], v[58:61]
	s_waitcnt vmcnt(7)
	v_cvt_f16_f32_e32 v26, v26
	v_mfma_f32_16x16x32_f16 v[62:65], v[82:85], v[78:81], v[62:65]
	ds_read_b128 v[70:73], v100 offset:40960
	ds_read_b128 v[74:77], v99 offset:10304
	ds_read_b128 v[78:81], v100 offset:41024
	v_cvt_pk_f16_f32 v27, v27, v28
	v_cvt_f16_f32_e32 v28, v29
	s_waitcnt vmcnt(6)
	v_cvt_f16_f32_e32 v29, v30
	v_cvt_pk_f16_f32 v30, v31, v32
	v_cvt_f16_f32_e32 v31, v33
	s_waitcnt vmcnt(5)
	v_cvt_f16_f32_e32 v32, v34
	v_cvt_pk_f16_f32 v33, v35, v36
	v_cvt_f16_f32_e32 v34, v37
	s_waitcnt vmcnt(4)
	v_cvt_f16_f32_e32 v35, v38
	v_cvt_f16_f32_e32 v37, v41
	s_waitcnt lgkmcnt(2)
	v_mfma_f32_16x16x32_f16 v[58:61], v[66:69], v[70:73], v[58:61]
	ds_read_b128 v[66:69], v99 offset:12800
	ds_read_b128 v[82:85], v99 offset:12864
	v_cvt_pk_f16_f32 v36, v39, v40
	v_pack_b32_f16 v26, v26, v27
	v_alignbit_b32 v27, v28, v27, 16
	v_pack_b32_f16 v28, v29, v30
	v_alignbit_b32 v29, v31, v30, 16
	v_pack_b32_f16 v30, v32, v33
	v_alignbit_b32 v31, v34, v33, 16
	v_pack_b32_f16 v32, v35, v36
	v_alignbit_b32 v33, v37, v36, 16
	ds_write2st64_b64 v98, v[26:27], v[28:29] offset1:10
	ds_write2st64_b64 v98, v[30:31], v[32:33] offset0:60 offset1:70
	s_waitcnt lgkmcnt(3)
	v_mfma_f32_16x16x32_f16 v[62:65], v[66:69], v[70:73], v[62:65]
	global_load_dwordx4 v[26:29], v[88:89], off offset:1536
	global_load_dwordx4 v[30:33], v[90:91], off offset:1536
	global_load_dwordx4 v[34:37], v[92:93], off offset:1536
	global_load_dwordx4 v[38:41], v[94:95], off offset:1536
	s_waitcnt lgkmcnt(0)
	s_barrier
	ds_read_b128 v[66:69], v99
	v_mfma_f32_16x16x32_f16 v[58:61], v[74:77], v[78:81], v[58:61]
	s_waitcnt vmcnt(6)
	v_cvt_f16_f32_e32 v49, v49
	s_waitcnt vmcnt(5)
	v_cvt_f16_f32_e32 v50, v50
	v_mfma_f32_16x16x32_f16 v[62:65], v[82:85], v[78:81], v[62:65]
	ds_read_b128 v[70:73], v100 offset:30720
	ds_read_b128 v[74:77], v99 offset:64
	ds_read_b128 v[78:81], v100 offset:30784
	global_load_dwordx4 v[82:85], v[88:89], off offset:1792
	ds_read_b128 v[86:89], v99 offset:2624
	s_waitcnt lgkmcnt(3)
	v_mfma_f32_16x16x32_f16 v[58:61], v[66:69], v[70:73], v[58:61]
	ds_read_b128 v[66:69], v99 offset:2560
	v_cvt_pk_f16_f32 v51, v51, v52
	v_cvt_f16_f32_e32 v52, v53
	s_waitcnt lgkmcnt(0)
	v_mfma_f32_16x16x32_f16 v[62:65], v[66:69], v[70:73], v[62:65]
	global_load_dwordx4 v[66:69], v[90:91], off offset:1792
	v_cvt_f16_f32_e32 v70, v42
	v_cvt_f16_f32_e32 v72, v45
	v_cvt_f16_f32_e32 v73, v46
	v_mfma_f32_16x16x32_f16 v[58:61], v[74:77], v[78:81], v[58:61]
	v_cvt_pk_f16_f32 v71, v43, v44
	v_cvt_pk_f16_f32 v74, v47, v48
	global_load_dwordx4 v[42:45], v[92:93], off offset:1792
	v_pack_b32_f16 v46, v70, v71
	v_alignbit_b32 v47, v72, v71, 16
	v_pack_b32_f16 v48, v73, v74
	v_alignbit_b32 v49, v49, v74, 16
	ds_write2st64_b64 v98, v[46:47], v[48:49] offset0:20 offset1:30
	global_load_dwordx4 v[46:49], v[94:95], off offset:1792
	s_waitcnt vmcnt(8)
	v_cvt_f16_f32_e32 v53, v54
	v_cvt_pk_f16_f32 v54, v55, v56
	v_cvt_f16_f32_e32 v55, v57
	v_pack_b32_f16 v50, v50, v51
	v_alignbit_b32 v51, v52, v51, 16
	v_pack_b32_f16 v52, v53, v54
	v_alignbit_b32 v53, v55, v54, 16
	ds_write2st64_b64 v98, v[50:51], v[52:53] offset0:80 offset1:90
	s_waitcnt lgkmcnt(0)
	s_barrier
	ds_read_b128 v[50:53], v99 offset:10240
	v_mfma_f32_16x16x32_f16 v[54:57], v[86:89], v[78:81], v[62:65]
	s_nop 2
	ds_read_b128 v[62:65], v100 offset:40960
	ds_read_b128 v[70:73], v99 offset:10304
	ds_read_b128 v[74:77], v100 offset:41024
	s_waitcnt vmcnt(7)
	v_cvt_f16_f32_e32 v26, v26
	v_cvt_pk_f16_f32 v27, v27, v28
	v_cvt_f16_f32_e32 v28, v29
	s_waitcnt vmcnt(6)
	v_cvt_f16_f32_e32 v29, v30
	v_cvt_pk_f16_f32 v30, v31, v32
	v_cvt_f16_f32_e32 v31, v33
	s_waitcnt vmcnt(5)
	v_cvt_f16_f32_e32 v32, v34
	v_cvt_pk_f16_f32 v33, v35, v36
	v_cvt_f16_f32_e32 v34, v37
	s_waitcnt vmcnt(4)
	v_cvt_f16_f32_e32 v35, v38
	v_cvt_f16_f32_e32 v37, v41
	s_waitcnt lgkmcnt(2)
	v_mfma_f32_16x16x32_f16 v[50:53], v[50:53], v[62:65], v[58:61]
	s_nop 2
	ds_read_b128 v[58:61], v99 offset:12800
	ds_read_b128 v[78:81], v99 offset:12864
	v_cvt_pk_f16_f32 v36, v39, v40
	v_pack_b32_f16 v26, v26, v27
	v_alignbit_b32 v27, v28, v27, 16
	v_pack_b32_f16 v28, v29, v30
	v_alignbit_b32 v29, v31, v30, 16
	s_waitcnt vmcnt(3)
	v_cvt_f16_f32_e32 v38, v82
	v_cvt_f16_f32_e32 v40, v85
	v_pack_b32_f16 v30, v32, v33
	v_alignbit_b32 v31, v34, v33, 16
	v_pack_b32_f16 v32, v35, v36
	v_alignbit_b32 v33, v37, v36, 16
	ds_write2st64_b64 v98, v[26:27], v[28:29] offset1:10
	ds_write2st64_b64 v98, v[30:31], v[32:33] offset0:60 offset1:70
	s_waitcnt lgkmcnt(0)
	s_barrier
	s_waitcnt vmcnt(2)
	v_cvt_f16_f32_e32 v41, v66
	ds_read_b128 v[26:29], v99
	v_mfma_f32_16x16x32_f16 v[54:57], v[58:61], v[62:65], v[54:57]
	v_cvt_pk_f16_f32 v39, v83, v84
	v_cvt_pk_f16_f32 v58, v67, v68
	v_pack_b32_f16 v62, v38, v39
	v_alignbit_b32 v63, v40, v39, 16
	v_pack_b32_f16 v64, v41, v58
	ds_read_b128 v[34:37], v99 offset:2560
	ds_read_b128 v[38:41], v100 offset:30720
	v_mfma_f32_16x16x32_f16 v[30:33], v[70:73], v[74:77], v[50:53]
	v_cvt_f16_f32_e32 v59, v69
	s_waitcnt vmcnt(1)
	v_cvt_f16_f32_e32 v42, v42
	v_cvt_pk_f16_f32 v43, v43, v44
	v_mfma_f32_16x16x32_f16 v[50:53], v[78:81], v[74:77], v[54:57]
	v_cvt_f16_f32_e32 v44, v45
	v_alignbit_b32 v65, v59, v58, 16
	s_nop 0
	ds_read_b128 v[54:57], v99 offset:64
	ds_read_b128 v[58:61], v100 offset:30784
	s_waitcnt lgkmcnt(2)
	v_mfma_f32_16x16x32_f16 v[26:29], v[26:29], v[38:41], v[30:33]
	v_mfma_f32_16x16x32_f16 v[34:37], v[34:37], v[38:41], v[50:53]
	s_waitcnt vmcnt(0)
	v_cvt_f16_f32_e32 v40, v46
	v_cvt_f16_f32_e32 v41, v49
	ds_read_b128 v[30:33], v99 offset:2624
	v_pack_b32_f16 v38, v42, v43
	v_cvt_pk_f16_f32 v42, v47, v48
	v_alignbit_b32 v39, v44, v43, 16
	v_pack_b32_f16 v40, v40, v42
	v_alignbit_b32 v41, v41, v42, 16
	ds_write2st64_b64 v98, v[62:63], v[64:65] offset0:20 offset1:30
	ds_write2st64_b64 v98, v[38:39], v[40:41] offset0:80 offset1:90
	s_waitcnt lgkmcnt(0)
	s_barrier
	ds_read_b128 v[38:41], v99 offset:10240
	v_mfma_f32_16x16x32_f16 v[26:29], v[54:57], v[58:61], v[26:29]
	v_mfma_f32_16x16x32_f16 v[30:33], v[30:33], v[58:61], v[34:37]
	s_nop 2
	ds_read_b128 v[34:37], v100 offset:40960
	ds_read_b128 v[42:45], v99 offset:10304
	ds_read_b128 v[46:49], v100 offset:41024
	s_waitcnt lgkmcnt(2)
	v_mfma_f32_16x16x32_f16 v[26:29], v[38:41], v[34:37], v[26:29]
	ds_read_b128 v[38:41], v99 offset:12800
	ds_read_b128 v[50:53], v99 offset:12864
	s_waitcnt vmcnt(0)
	s_waitcnt lgkmcnt(0)
	v_mfma_f32_16x16x32_f16 v[26:29], v[42:45], v[46:49], v[26:29]
	v_or_b32_e32 v18, v23, v24
	v_mul_u32_u24_e32 v18, 0xa0, v18
	v_lshl_add_u32 v18, v1, 1, v18
	v_mfma_f32_16x16x32_f16 v[30:33], v[38:41], v[34:37], v[30:33]
	s_barrier
	s_nop 2
	v_add_f32_e32 v19, v26, v97
	v_cvt_f16_f32_e32 v19, v19
	v_mfma_f32_16x16x32_f16 v[30:33], v[50:53], v[46:49], v[30:33]
	v_add_f32_e32 v20, v27, v97
	v_cvt_f16_f32_e32 v20, v20
	v_add_f32_e32 v21, v28, v97
	v_cvt_f16_f32_e32 v21, v21
	v_add_f32_e32 v26, v29, v97
	v_cvt_f16_f32_e32 v26, v26
	ds_write_b16 v18, v19
	ds_write_b16 v18, v20 offset:160
	ds_write_b16 v18, v21 offset:320
	ds_write_b16 v18, v26 offset:480
	v_add_f32_e32 v19, v30, v97
	v_cvt_f16_f32_e32 v19, v19
	v_add_f32_e32 v20, v31, v97
	v_cvt_f16_f32_e32 v20, v20
	v_add_f32_e32 v21, v32, v97
	v_cvt_f16_f32_e32 v21, v21
	v_add_f32_e32 v26, v33, v97
	v_cvt_f16_f32_e32 v26, v26
	ds_write_b16 v18, v19 offset:2560
	ds_write_b16 v18, v20 offset:2720
	ds_write_b16 v18, v21 offset:2880
	ds_write_b16 v18, v26 offset:3040
	s_waitcnt lgkmcnt(0)
	s_barrier
	ds_read_b128 v[18:21], v99
	v_cvt_pk_f16_f32 v17, v16, v17
	v_cvt_pk_f16_f32 v16, v14, v15
	v_cvt_pk_f16_f32 v15, v8, v9
	v_cvt_pk_f16_f32 v14, v6, v7
	ds_read_b128 v[6:9], v99 offset:64
	ds_read_b128 v[26:29], v99 offset:2560
	ds_read_b128 v[30:33], v99 offset:2624
	s_waitcnt lgkmcnt(3)
	v_mfma_f32_16x16x32_f16 v[18:21], v[18:21], v[14:17], 0
	v_cvt_pk_f16_f32 v13, v12, v13
	v_cvt_pk_f16_f32 v12, v10, v11
	v_cvt_pk_f16_f32 v11, v4, v5
	s_waitcnt lgkmcnt(1)
	v_mfma_f32_16x16x32_f16 v[14:17], v[26:29], v[14:17], 0
	v_cvt_pk_f16_f32 v10, v2, v3
	s_nop 1
	v_mfma_f32_16x16x32_f16 v[2:5], v[6:9], v[10:13], v[18:21]
	s_waitcnt lgkmcnt(0)
	v_mfma_f32_16x16x32_f16 v[6:9], v[30:33], v[10:13], v[14:17]
	v_or3_b32 v12, s2, v24, v23
	v_lshlrev_b32_e32 v24, 3, v1
	v_lshl_add_u64 v[10:11], s[0:1], 0, v[24:25]
	s_nop 2
	v_add_f32_e32 v1, v96, v2
	s_mov_b32 s0, 0xc2200000
	v_mov_b32_e32 v14, 0x42200000
	v_med3_f32 v1, v1, s0, v14
	v_mul_f32_e32 v1, 0x4038aa3b, v1
	v_exp_f32_e32 v2, v1
	v_add_f32_e32 v1, v96, v3
	v_med3_f32 v1, v1, s0, v14
	v_mul_f32_e32 v1, 0x4038aa3b, v1
	s_mul_i32 s2, s6, 0xc0
	v_exp_f32_e32 v3, v1
	v_lshrrev_b32_e32 v1, 1, v12
	v_add_u32_e32 v24, s2, v1
	v_add_f32_e32 v1, v96, v4
	v_med3_f32 v1, v1, s0, v14
	v_mul_f32_e32 v1, 0x4038aa3b, v1
	v_exp_f32_e32 v4, v1
	v_add_f32_e32 v1, v96, v5
	v_med3_f32 v1, v1, s0, v14
	v_mul_f32_e32 v1, 0x4038aa3b, v1
	v_exp_f32_e32 v5, v1
	v_add_f32_e32 v1, v96, v6
	v_med3_f32 v1, v1, s0, v14
	v_mul_f32_e32 v1, 0x4038aa3b, v1
	v_exp_f32_e32 v6, v1
	v_add_f32_e32 v1, v96, v7
	v_med3_f32 v1, v1, s0, v14
	v_mul_f32_e32 v1, 0x4038aa3b, v1
	v_lshlrev_b64 v[12:13], 9, v[24:25]
	v_exp_f32_e32 v7, v1
	v_add_f32_e32 v1, v96, v8
	v_lshl_add_u64 v[12:13], v[10:11], 0, v[12:13]
	v_med3_f32 v1, v1, s0, v14
	global_store_dwordx2 v[12:13], v[2:3], off
	v_or_b32_e32 v12, 1, v24
	v_mov_b32_e32 v13, v25
	v_mul_f32_e32 v1, 0x4038aa3b, v1
	v_lshlrev_b64 v[12:13], 9, v[12:13]
	v_exp_f32_e32 v8, v1
	v_add_f32_e32 v1, v96, v9
	v_lshl_add_u64 v[12:13], v[10:11], 0, v[12:13]
	v_med3_f32 v1, v1, s0, v14
	global_store_dwordx2 v[12:13], v[4:5], off
	v_or_b32_e32 v12, 8, v24
	v_mov_b32_e32 v13, v25
	v_mul_f32_e32 v1, 0x4038aa3b, v1
	v_lshlrev_b64 v[12:13], 9, v[12:13]
	v_exp_f32_e32 v9, v1
	v_lshl_add_u64 v[12:13], v[10:11], 0, v[12:13]
	v_or_b32_e32 v24, 9, v24
	global_store_dwordx2 v[12:13], v[6:7], off
	v_lshlrev_b64 v[12:13], 9, v[24:25]
	v_lshl_add_u64 v[10:11], v[10:11], 0, v[12:13]
	global_store_dwordx2 v[10:11], v[8:9], off
	v_mbcnt_lo_u32_b32 v10, -1, 0
	s_and_saveexec_b64 s[0:1], vcc
	s_xor_b64 s[0:1], exec, s[0:1]
	v_mbcnt_hi_u32_b32 v1, -1, v10
	v_and_b32_e32 v10, 64, v1
	v_add_u32_e32 v14, 64, v10
	v_xor_b32_e32 v15, 32, v1
	v_xor_b32_e32 v16, 16, v1
	v_xor_b32_e32 v18, 8, v1
	v_xor_b32_e32 v19, 4, v1
	v_xor_b32_e32 v20, 2, v1
	v_xor_b32_e32 v21, 1, v1
	s_or_saveexec_b64 s[0:1], s[0:1]
	v_and_b32_e32 v17, 63, v0
	s_xor_b64 exec, exec, s[0:1]
	s_cmp_gt_u32 s88, 7
	s_cbranch_scc1 .LBB0_23
	s_cbranch_execz .LBB0_23
	v_mbcnt_hi_u32_b32 v1, -1, v10
	v_and_b32_e32 v10, 64, v1
	v_add_u32_e32 v14, 64, v10
	v_xor_b32_e32 v15, 32, v1
	v_cmp_lt_i32_e32 vcc, v15, v14
	v_and_b32_e32 v23, 0x7fffffff, v22
	v_xor_b32_e32 v16, 16, v1
	v_cndmask_b32_e32 v10, v1, v15, vcc
	v_lshlrev_b32_e32 v11, 2, v10
	ds_bpermute_b32 v10, v11, v22
	ds_bpermute_b32 v11, v11, v23
	v_cmp_lt_i32_e32 vcc, v16, v14
	v_xor_b32_e32 v18, 8, v1
	s_waitcnt lgkmcnt(0)
	v_pk_add_f32 v[10:11], v[22:23], v[10:11]
	v_cndmask_b32_e32 v12, v1, v16, vcc
	v_lshlrev_b32_e32 v13, 2, v12
	ds_bpermute_b32 v12, v13, v10
	ds_bpermute_b32 v13, v13, v11
	v_cmp_lt_i32_e32 vcc, v18, v14
	s_waitcnt lgkmcnt(0)
	v_pk_add_f32 v[10:11], v[10:11], v[12:13]
	v_cndmask_b32_e32 v19, v1, v18, vcc
	v_lshlrev_b32_e32 v19, 2, v19
	ds_bpermute_b32 v12, v19, v10
	ds_bpermute_b32 v13, v19, v11
	v_xor_b32_e32 v19, 4, v1
	v_cmp_lt_i32_e32 vcc, v19, v14
	s_waitcnt lgkmcnt(0)
	v_pk_add_f32 v[10:11], v[10:11], v[12:13]
	v_cndmask_b32_e32 v20, v1, v19, vcc
	v_lshlrev_b32_e32 v20, 2, v20
	ds_bpermute_b32 v12, v20, v10
	ds_bpermute_b32 v13, v20, v11
	v_xor_b32_e32 v20, 2, v1
	v_cmp_lt_i32_e32 vcc, v20, v14
	s_waitcnt lgkmcnt(0)
	v_pk_add_f32 v[10:11], v[10:11], v[12:13]
	v_cndmask_b32_e32 v21, v1, v20, vcc
	v_lshlrev_b32_e32 v21, 2, v21
	ds_bpermute_b32 v12, v21, v10
	ds_bpermute_b32 v13, v21, v11
	v_xor_b32_e32 v21, 1, v1
	v_cmp_lt_i32_e32 vcc, v21, v14
	s_waitcnt lgkmcnt(0)
	v_pk_add_f32 v[10:11], v[10:11], v[12:13]
	v_cndmask_b32_e32 v12, v1, v21, vcc
	v_lshlrev_b32_e32 v13, 2, v12
	ds_bpermute_b32 v12, v13, v10
	ds_bpermute_b32 v13, v13, v11
	v_cmp_eq_u32_e32 vcc, 0, v17
	s_and_saveexec_b64 s[2:3], vcc
	s_cbranch_execz .LBB0_22
	v_mov_b32_e32 v22, 0
	s_waitcnt lgkmcnt(0)
	v_pk_add_f32 v[10:11], v[10:11], v[12:13]
	global_store_dwordx2 v22, v[10:11], s[4:5] offset:1024
